# loop-header offset copies for the next odd-step pieces reduced from four 64-bit to four 32-bit moves (the LDS-DMA pieces only read the low dwords now), four GEMM K-loops
# baseline (speedup 1.0000x reference)
.LBB0_102:
	s_cmpk_eq_i32 s66, 0xf00
	s_cselect_b64 s[68:69], -1, 0
	s_cmpk_lg_i32 s66, 0xf00
	v_mov_b32_e32 v160, v134
	v_mov_b32_e32 v162, v132
	v_mov_b32_e32 v164, v130
	v_mov_b32_e32 v166, v146
	s_cbranch_scc1 .LBB0_101
	s_andn2_b64 vcc, exec, s[0:1]
	v_mov_b32_e32 v180, v132
	v_mov_b32_e32 v181, v134
	v_mov_b32_e32 v182, v146
	v_mov_b32_e32 v183, v130
	v_mov_b64_e32 v[166:167], v[146:147]
	v_mov_b64_e32 v[164:165], v[130:131]
	v_mov_b64_e32 v[162:163], v[132:133]
	v_mov_b64_e32 v[160:161], v[134:135]
	s_cbranch_vccnz .LBB0_101
	v_mov_b32_e32 v180, v138
	v_mov_b32_e32 v181, v150
	v_mov_b32_e32 v182, v136
	v_mov_b32_e32 v183, v140
	v_mov_b64_e32 v[166:167], v[136:137]
	v_mov_b64_e32 v[164:165], v[140:141]
	v_mov_b64_e32 v[162:163], v[138:139]
	v_mov_b64_e32 v[160:161], v[150:151]
	s_branch .LBB0_101

.LBB0_386:
	s_cmpk_eq_i32 s28, 0xf00
	s_cselect_b64 s[30:31], -1, 0
	s_cmpk_lg_i32 s28, 0xf00
	v_mov_b32_e32 v160, v134
	v_mov_b32_e32 v162, v132
	v_mov_b32_e32 v164, v130
	v_mov_b32_e32 v166, v150
	s_cbranch_scc1 .LBB0_385
	s_andn2_b64 vcc, exec, s[0:1]
	v_mov_b32_e32 v179, v132
	v_mov_b32_e32 v180, v134
	v_mov_b32_e32 v181, v150
	v_mov_b32_e32 v182, v130
	v_mov_b64_e32 v[166:167], v[150:151]
	v_mov_b64_e32 v[164:165], v[130:131]
	v_mov_b64_e32 v[162:163], v[132:133]
	v_mov_b64_e32 v[160:161], v[134:135]
	s_cbranch_vccnz .LBB0_385
	v_mov_b32_e32 v179, v138
	v_mov_b32_e32 v180, v142
	v_mov_b32_e32 v181, v136
	v_mov_b32_e32 v182, v140
	v_mov_b64_e32 v[166:167], v[136:137]
	v_mov_b64_e32 v[164:165], v[140:141]
	v_mov_b64_e32 v[162:163], v[138:139]
	v_mov_b64_e32 v[160:161], v[142:143]
	s_branch .LBB0_385

.LBB0_778:
	s_cmpk_eq_i32 s40, 0x700
	s_cselect_b64 s[42:43], -1, 0
	s_cmpk_lg_i32 s40, 0x700
	v_mov_b32_e32 v192, v182
	v_mov_b32_e32 v194, v180
	v_mov_b32_e32 v196, v178
	v_mov_b32_e32 v198, v176
	s_cbranch_scc1 .Lp6_idx_chk
	s_andn2_b64 vcc, exec, s[0:1]
	v_cndmask_b32_e32 v172, v172, v180, vcc
	v_cndmask_b32_e32 v174, v174, v182, vcc
	v_cndmask_b32_e32 v162, v162, v176, vcc
	v_cndmask_b32_e32 v170, v170, v178, vcc
	v_mov_b64_e32 v[198:199], v[176:177]
	v_mov_b64_e32 v[196:197], v[178:179]
	v_mov_b64_e32 v[194:195], v[180:181]
	v_mov_b64_e32 v[192:193], v[182:183]
	s_cbranch_vccnz .LBB0_777
	v_mov_b32_e32 v171, v163
	v_mov_b32_e32 v173, v163
	v_mov_b32_e32 v175, v163
	v_lshl_or_b32 v162, v162, 11, v205
	v_lshl_or_b32 v172, v172, 11, v205
	v_lshl_or_b32 v170, v170, 11, v206
	v_lshl_or_b32 v174, v174, 11, v206
	v_mov_b64_e32 v[198:199], v[162:163]
	v_mov_b64_e32 v[196:197], v[170:171]
	v_mov_b64_e32 v[194:195], v[172:173]
	v_mov_b64_e32 v[192:193], v[174:175]
	s_branch .LBB0_777

.LBB0_863:
	s_cmpk_eq_i32 s44, 0x700
	s_cselect_b64 s[46:47], -1, 0
	s_cmpk_lg_i32 s44, 0x700
	v_mov_b32_e32 v192, v174
	v_mov_b32_e32 v194, v172
	v_mov_b32_e32 v196, v170
	v_mov_b32_e32 v198, v166
	s_cbranch_scc1 .LBB0_862
	s_andn2_b64 vcc, exec, s[0:1]
	v_mov_b32_e32 v216, v172
	v_mov_b32_e32 v217, v174
	v_mov_b32_e32 v218, v166
	v_mov_b32_e32 v219, v170
	v_mov_b64_e32 v[198:199], v[166:167]
	v_mov_b64_e32 v[196:197], v[170:171]
	v_mov_b64_e32 v[194:195], v[172:173]
	v_mov_b64_e32 v[192:193], v[174:175]
	s_cbranch_vccnz .LBB0_862
	v_mov_b32_e32 v216, v178
	v_mov_b32_e32 v217, v182
	v_mov_b32_e32 v218, v176
	v_mov_b32_e32 v219, v180
	v_mov_b64_e32 v[198:199], v[176:177]
	v_mov_b64_e32 v[196:197], v[180:181]
	v_mov_b64_e32 v[194:195], v[178:179]
	v_mov_b64_e32 v[192:193], v[182:183]
	s_branch .LBB0_862
